# P2 stage D1: forward-substitution rows 1..11 read ahead through an 11-quad register ring with counted lgkmcnt (was read->lgkmcnt(0)->chain per row pair); stacked
# baseline (speedup 1.0000x reference)
.LBB0_407:
	s_andn2_b64 vcc, exec, s[94:95]
	s_cbranch_vccnz .LBB0_443
	v_mov_b32_e32 v1, s9
	ds_read_b128 v[4:7], v1 offset:256
	ds_read_b128 v[8:11], v1 offset:512
	ds_read_b128 v[12:15], v1 offset:768
	ds_read_b128 v[150:153], v1 offset:1024
	ds_read_b128 v[154:157], v1 offset:1280
	ds_read_b128 v[158:161], v1 offset:1296
	ds_read_b128 v[228:231], v1 offset:1536
	ds_read_b128 v[232:235], v1 offset:1552
	ds_read_b128 v[236:239], v1 offset:1792
	ds_read_b128 v[240:243], v1 offset:1808
	ds_read_b128 v[244:247], v1 offset:2048
	v_and_b32_e32 v16, 15, v186
	v_cmp_eq_u32_e32 vcc, 0, v16
	v_bfe_u32 v2, v186, 4, 2
	s_mov_b64 s[70:71], s[96:97]
	v_cndmask_b32_e64 v211, 0, 1.0, vcc
	v_cmp_eq_u32_e32 vcc, 1, v16
	s_waitcnt lgkmcnt(10)
	v_fma_f32 v252, v211, v4, 0
	s_nop 1
	v_cndmask_b32_e64 v248, 0, 1.0, vcc
	v_sub_f32_e32 v212, v248, v252
	ds_read_b128 v[4:7], v1 offset:2064
	v_cmp_eq_u32_e32 vcc, 2, v16
	s_waitcnt lgkmcnt(10)
	v_fma_f32 v252, v211, v8, 0
	v_fma_f32 v253, v9, v212, 0
	v_add_f32_e32 v252, v252, v253
	v_cndmask_b32_e64 v248, 0, 1.0, vcc
	v_sub_f32_e32 v213, v248, v252
	ds_read_b128 v[8:11], v1 offset:2304
	v_cmp_eq_u32_e32 vcc, 3, v16
	s_waitcnt lgkmcnt(10)
	v_fma_f32 v252, v211, v12, 0
	v_fma_f32 v253, v13, v212, 0
	v_fmac_f32_e32 v252, v14, v213
	v_add_f32_e32 v252, v252, v253
	v_cndmask_b32_e64 v248, 0, 1.0, vcc
	v_sub_f32_e32 v17, v248, v252
	ds_read_b128 v[12:15], v1 offset:2320
	v_cmp_eq_u32_e32 vcc, 4, v16
	s_waitcnt lgkmcnt(10)
	v_fma_f32 v252, v211, v150, 0
	v_fma_f32 v253, v151, v212, 0
	v_fmac_f32_e32 v252, v152, v213
	v_fmac_f32_e32 v253, v153, v17
	v_add_f32_e32 v252, v252, v253
	v_cndmask_b32_e64 v248, 0, 1.0, vcc
	v_sub_f32_e32 v214, v248, v252
	ds_read_b128 v[150:153], v1 offset:2336
	v_cmp_eq_u32_e32 vcc, 5, v16
	s_waitcnt lgkmcnt(9)
	v_fma_f32 v252, v211, v154, 0
	v_fma_f32 v253, v155, v212, 0
	v_fmac_f32_e32 v252, v156, v213
	v_fmac_f32_e32 v253, v157, v17
	v_fmac_f32_e32 v252, v158, v214
	v_add_f32_e32 v252, v252, v253
	v_cndmask_b32_e64 v248, 0, 1.0, vcc
	v_sub_f32_e32 v215, v248, v252
	ds_read_b128 v[154:157], v1 offset:2560
	ds_read_b128 v[158:161], v1 offset:2576
	v_cmp_eq_u32_e32 vcc, 6, v16
	s_waitcnt lgkmcnt(9)
	v_fma_f32 v252, v211, v228, 0
	v_fma_f32 v253, v229, v212, 0
	v_fmac_f32_e32 v252, v230, v213
	v_fmac_f32_e32 v253, v231, v17
	v_fmac_f32_e32 v252, v232, v214
	v_fmac_f32_e32 v253, v233, v215
	v_add_f32_e32 v252, v252, v253
	v_cndmask_b32_e64 v248, 0, 1.0, vcc
	v_sub_f32_e32 v217, v248, v252
	ds_read_b128 v[228:231], v1 offset:2592
	ds_read_b128 v[232:235], v1 offset:2816
	v_cmp_eq_u32_e32 vcc, 7, v16
	s_waitcnt lgkmcnt(9)
	v_fma_f32 v252, v211, v236, 0
	v_fma_f32 v253, v237, v212, 0
	v_fmac_f32_e32 v252, v238, v213
	v_fmac_f32_e32 v253, v239, v17
	v_fmac_f32_e32 v252, v240, v214
	v_fmac_f32_e32 v253, v241, v215
	v_fmac_f32_e32 v252, v242, v217
	v_add_f32_e32 v252, v252, v253
	v_cndmask_b32_e64 v248, 0, 1.0, vcc
	v_sub_f32_e32 v216, v248, v252
	ds_read_b128 v[236:239], v1 offset:2832
	ds_read_b128 v[240:243], v1 offset:2848
	v_cmp_eq_u32_e32 vcc, 8, v16
	s_waitcnt lgkmcnt(9)
	v_fma_f32 v252, v211, v244, 0
	v_fma_f32 v253, v245, v212, 0
	v_fmac_f32_e32 v252, v246, v213
	v_fmac_f32_e32 v253, v247, v17
	v_fmac_f32_e32 v252, v4, v214
	v_fmac_f32_e32 v253, v5, v215
	v_fmac_f32_e32 v252, v6, v217
	v_fmac_f32_e32 v253, v7, v216
	v_add_f32_e32 v252, v252, v253
	v_cndmask_b32_e64 v248, 0, 1.0, vcc
	v_sub_f32_e32 v219, v248, v252
	v_cmp_eq_u32_e32 vcc, 9, v16
	s_waitcnt lgkmcnt(6)
	v_fma_f32 v252, v211, v8, 0
	v_fma_f32 v253, v9, v212, 0
	v_fmac_f32_e32 v252, v10, v213
	v_fmac_f32_e32 v253, v11, v17
	v_fmac_f32_e32 v252, v12, v214
	v_fmac_f32_e32 v253, v13, v215
	v_fmac_f32_e32 v252, v14, v217
	v_fmac_f32_e32 v253, v15, v216
	v_fmac_f32_e32 v252, v150, v219
	v_add_f32_e32 v252, v252, v253
	v_cndmask_b32_e64 v248, 0, 1.0, vcc
	v_sub_f32_e32 v220, v248, v252
	v_cmp_eq_u32_e32 vcc, 10, v16
	s_waitcnt lgkmcnt(3)
	v_fma_f32 v252, v211, v154, 0
	v_fma_f32 v253, v155, v212, 0
	v_fmac_f32_e32 v252, v156, v213
	v_fmac_f32_e32 v253, v157, v17
	v_fmac_f32_e32 v252, v158, v214
	v_fmac_f32_e32 v253, v159, v215
	v_fmac_f32_e32 v252, v160, v217
	v_fmac_f32_e32 v253, v161, v216
	v_fmac_f32_e32 v252, v228, v219
	v_fmac_f32_e32 v253, v229, v220
	v_add_f32_e32 v252, v252, v253
	v_cndmask_b32_e64 v248, 0, 1.0, vcc
	v_sub_f32_e32 v221, v248, v252
	v_cmp_eq_u32_e32 vcc, 11, v16
	s_waitcnt lgkmcnt(0)
	v_fma_f32 v252, v211, v232, 0
	v_fma_f32 v253, v233, v212, 0
	v_fmac_f32_e32 v252, v234, v213
	v_fmac_f32_e32 v253, v235, v17
	v_fmac_f32_e32 v252, v236, v214
	v_fmac_f32_e32 v253, v237, v215
	v_fmac_f32_e32 v252, v238, v217
	v_fmac_f32_e32 v253, v239, v216
	v_fmac_f32_e32 v252, v240, v219
	v_fmac_f32_e32 v253, v241, v220
	v_fmac_f32_e32 v252, v242, v221
	v_add_f32_e32 v252, v252, v253
	v_cndmask_b32_e64 v248, 0, 1.0, vcc
	v_sub_f32_e32 v222, v248, v252
	ds_read_b128 v[4:7], v1 offset:3072
	ds_read_b128 v[8:11], v1 offset:3088
	ds_read_b128 v[12:15], v1 offset:3104
	ds_read_b128 v[182:185], v1 offset:3328
	ds_read_b128 v[178:181], v1 offset:3344
	ds_read_b128 v[174:177], v1 offset:3360
	ds_read_b128 v[170:173], v1 offset:3376
	s_waitcnt lgkmcnt(6)
	v_fma_f32 v4, v211, v4, 0
	v_fma_f32 v5, v212, v5, 0
	v_fmac_f32_e32 v4, v213, v6
	v_fmac_f32_e32 v5, v17, v7
	s_waitcnt lgkmcnt(5)
	v_fmac_f32_e32 v4, v214, v8
	v_fmac_f32_e32 v5, v215, v9
	v_fmac_f32_e32 v4, v10, v217
	v_fmac_f32_e32 v5, v11, v216
	s_waitcnt lgkmcnt(4)
	v_fmac_f32_e32 v4, v12, v219
	v_fmac_f32_e32 v5, v13, v220
	v_fmac_f32_e32 v4, v14, v221
	v_fmac_f32_e32 v5, v15, v222
	v_cmp_eq_u32_e32 vcc, 12, v16
	v_add_f32_e32 v4, v4, v5
	s_nop 0
	v_cndmask_b32_e64 v6, 0, 1.0, vcc
	s_waitcnt lgkmcnt(0)
	v_sub_f32_e32 v171, v6, v4
	ds_read_b128 v[166:169], v1 offset:3584
	ds_read_b128 v[162:165], v1 offset:3600
	ds_read_b128 v[158:161], v1 offset:3616
	ds_read_b128 v[154:157], v1 offset:3632
	ds_read_b128 v[150:153], v1 offset:3840
	ds_read_b128 v[12:15], v1 offset:3856
	ds_read_b128 v[8:11], v1 offset:3872
	ds_read_b128 v[4:7], v1 offset:3888
	v_cmp_lt_i32_e32 vcc, 1, v2
	s_and_saveexec_b64 s[94:95], vcc
	s_xor_b64 s[94:95], exec, s[94:95]
	s_cbranch_execz .LBB0_412
	v_cmp_lt_i32_e32 vcc, 2, v2
	s_and_saveexec_b64 s[96:97], vcc
	s_xor_b64 s[96:97], exec, s[96:97]
	s_or_saveexec_b64 s[96:97], s[96:97]
	v_mov_b32_e32 v223, v171
	s_xor_b64 exec, exec, s[96:97]
	v_mov_b32_e32 v223, v219
	s_or_b64 exec, exec, s[96:97]
